# attention K/V staging by LDS-DMA (global_load_lds_dwordx4, 3-stage ring, source-side swizzled row-major K image) instead of register staging + ds_write
# speedup vs baseline: 1.0369x; 1.0119x over previous
; __device__ __forceinline__ int lane_id() { unsigned z = 0u; asm volatile("" : "+v"(z)); return (int)__builtin_amdgcn_mbcnt_hi(~0u, __builtin_amdgcn_mbcnt_lo(~0u, z)); }
; __device__ __forceinline__ void attn_unit(const Frame& F, const bf16* __restrict__ proj, bf16* mix, const float* relb, const float* subg, int h, int qb, float lam, float one_m_li) {
;     ...
;     int tid = F.wave * 64 + lane_id(); asm volatile("" : "+v"(tid));
;     const int lane = tid & 63, w = F.wave, r32 = lane & 31, hi = lane >> 5, m = w >> 2, wq = w & 3;
;     const int q0 = qb * 128, qrow = q0 + 32 * wq + r32, cw = (q0 + 32 * wq) >> 6, NT = 2 * qb + 2;
; __global__ void __launch_bounds__(NTHR, 2) fwd(Args args) {
;     ...
;                 int ln_ = lane_id(); asm volatile("" : "+v"(ln_));
;                 float d1 = ka->in[18][l * 64 + ln_] * ka->in[19][l * 64 + ln_], d2 = ka->in[20][l * 64 + ln_] * ka->in[21][l * 64 + ln_];
;                 d1 = wave_sum(d1); d2 = wave_sum(d2);
;                 const float lam_init = (l == 0) ? 0.2f : 0.35550906f;
;                 const float lam = expf(d1) - expf(d2) + lam_init;
.LBB0_559:
	s_waitcnt vmcnt(0)
	v_mov_b32_e32 v0, v193
	s_cmpk_lt_i32 s2, 0x100
	v_mbcnt_lo_u32_b32 v0, -1, v0
	v_mbcnt_hi_u32_b32 v0, -1, v0
	s_load_dwordx8 s[44:51], s[8:9], 0x90
	v_lshl_add_u32 v0, s78, 6, v0
	v_ashrrev_i32_e32 v1, 31, v0
	v_lshlrev_b64 v[0:1], 2, v[0:1]
	s_waitcnt lgkmcnt(0)
	v_lshl_add_u64 v[2:3], s[44:45], 0, v[0:1]
	global_load_dword v4, v[2:3], off
	v_lshl_add_u64 v[2:3], s[46:47], 0, v[0:1]
	global_load_dword v5, v[2:3], off
	v_lshl_add_u64 v[2:3], s[48:49], 0, v[0:1]
	v_lshl_add_u64 v[0:1], s[50:51], 0, v[0:1]
	global_load_dword v2, v[2:3], off
	v_mov_b32_e32 v3, v193
	global_load_dword v0, v[0:1], off
	v_mov_b32_e32 v1, v193
	s_waitcnt vmcnt(2)
	v_mul_f32_e32 v6, v4, v5
	s_nop 1
	v_mov_b32_dpp v1, v6 quad_perm:[1,0,3,2] row_mask:0xf bank_mask:0xf
	v_fmac_f32_e32 v1, v4, v5
	s_waitcnt vmcnt(0)
	v_mul_f32_e32 v7, v2, v0
	s_nop 1
	v_mov_b32_dpp v3, v7 quad_perm:[1,0,3,2] row_mask:0xf bank_mask:0xf
	v_fmac_f32_e32 v3, v2, v0
	v_add_f32_dpp v0, v1, v1 quad_perm:[2,3,0,1] row_mask:0xf bank_mask:0xf bound_ctrl:1
	s_nop 0
	v_add_f32_dpp v1, v3, v3 quad_perm:[2,3,0,1] row_mask:0xf bank_mask:0xf bound_ctrl:1
	v_add_f32_dpp v0, v0, v0 row_half_mirror row_mask:0xf bank_mask:0xf bound_ctrl:1
	s_nop 0
	v_add_f32_dpp v1, v1, v1 row_half_mirror row_mask:0xf bank_mask:0xf bound_ctrl:1
	v_add_f32_dpp v0, v0, v0 row_mirror row_mask:0xf bank_mask:0xf bound_ctrl:1
	v_mov_b32_e32 v2, v0
	v_add_f32_dpp v1, v1, v1 row_mirror row_mask:0xf bank_mask:0xf bound_ctrl:1
	v_mov_b32_e32 v3, v1
	s_nop 1
	v_permlane32_swap_b32 v0, v2
	s_nop 1
	v_permlane32_swap_b32 v1, v3
	s_nop 0
	v_add_f32_e32 v0, v0, v2
	v_add_f32_e32 v1, v1, v3
	v_readlane_b32 s4, v0, 0
	v_readlane_b32 s6, v0, 16
	v_readlane_b32 s5, v1, 0
	v_readlane_b32 s7, v1, 16
	s_cbranch_scc0 .LBB0_596
	v_mov_b32_e32 v0, s6
	v_add_f32_e32 v0, s4, v0
	v_mov_b32_e32 v2, 0x3eb60549
	v_mov_b32_e32 v3, 0x3e4ccccd
	v_cndmask_b32_e64 v2, v2, v3, s[36:37]
	v_mul_f32_e32 v3, 0x3fb8aa3b, v0
	s_mov_b32 s4, 0x3fb8aa3b
	v_fma_f32 v4, v0, s4, -v3
	v_rndne_f32_e32 v5, v3
	v_fmac_f32_e32 v4, 0x32a5705f, v0
	v_sub_f32_e32 v3, v3, v5
	v_add_f32_e32 v3, v3, v4
	v_exp_f32_e32 v3, v3
	v_cvt_i32_f32_e32 v4, v5
	v_mov_b32_e32 v1, s7
	v_add_f32_e32 v1, s5, v1
	s_mov_b32 s5, 0xc2ce8ed0
	v_ldexp_f32 v3, v3, v4
	v_cmp_ngt_f32_e32 vcc, s5, v0
	s_mov_b32 s6, 0x42b17218
	v_mov_b32_e32 v6, 0x7f800000
	v_cndmask_b32_e32 v3, 0, v3, vcc
	v_cmp_nlt_f32_e32 vcc, s6, v0
	s_lshl_b32 s100, s12, 11
	s_and_b32 s10, s12, 3
	s_lshl_b32 s24, s12, 6
	v_cndmask_b32_e32 v0, v6, v3, vcc
	v_mul_f32_e32 v3, 0x3fb8aa3b, v1
	v_fma_f32 v4, v1, s4, -v3
	v_rndne_f32_e32 v5, v3
	v_fmac_f32_e32 v4, 0x32a5705f, v1
	v_sub_f32_e32 v3, v3, v5
	v_add_f32_e32 v3, v3, v4
	v_exp_f32_e32 v3, v3
	v_cvt_i32_f32_e32 v4, v5
	v_cmp_ngt_f32_e32 vcc, s5, v1
	s_lshl_b32 s29, s10, 5
	s_load_dwordx4 s[36:39], s[8:9], 0xb0
	v_ldexp_f32 v3, v3, v4
	v_cndmask_b32_e32 v3, 0, v3, vcc
	v_cmp_nlt_f32_e32 vcc, s6, v1
	s_ashr_i32 s6, s12, 2
	s_lshl_b32 s4, s6, 6
	s_ashr_i32 s5, s4, 31
	s_add_u32 s30, s42, 0x39101c00
	s_addc_u32 s31, s43, 0
	s_add_u32 s34, s42, 0x39102000
	s_addc_u32 s35, s43, 0
	s_lshl_b32 s40, s6, 13
	s_add_i32 s41, s40, 0
	s_cmp_eq_u32 s6, 1
	s_cselect_b64 s[6:7], -1, 0
	s_lshl_b32 s11, s10, 14
	s_add_i32 s53, s11, 0
	s_cmp_lt_u32 s12, 4
	s_cselect_b64 s[44:45], -1, 0
	s_lshl_b32 s11, s12, 14
	s_lshl_b32 s60, s78, 7
	v_cndmask_b32_e32 v1, v6, v3, vcc
	s_add_i32 s56, s11, 0
	s_lshl_b64 s[8:9], s[60:61], 2
	v_sub_f32_e32 v0, v0, v1
	s_waitcnt lgkmcnt(0)
	s_add_u32 s36, s36, s8
	v_add_f32_e32 v160, v2, v0
	s_addc_u32 s37, s37, s9
	s_lshl_b32 s8, s10, 7
	v_sub_f32_e32 v186, 1.0, v2
	v_mov_b32_e32 v161, v160
	s_sub_i32 s57, 0, s8
	s_branch .LBB0_562

; #define LAS __attribute__((address_space(3)))
; #define AT_LOAD(j) do { _Pragma("unroll") for (int i = 0; i < 2; ++i) { const int id = tid + 512 * i, row = id >> 4, c16 = id & 15; \
;         rk[i] = *(const u32x4*)(kbase + (size_t)(64 * (j) + row) * PW + c16 * 8); rv[i] = *(const u32x4*)(vbase + (size_t)(64 * (j) + row) * PW + c16 * 8); } } while (0)
; #define AT_STORE(buf) do { _Pragma("unroll") for (int i = 0; i < 2; ++i) { const int id = tid + 512 * i, row = id >> 4, c16 = id & 15, mk = c16 >> 3, c = c16 & 7; \
;         *(LAS u32x4*)(lds + (buf) * STAGE + mk * 8192 + c * 1024 + ((row ^ c) * 16)) = rk[i]; \
;         *(LAS u32x4*)(lds + (buf) * STAGE + 16384 + (c16 >> 2) * 4096 + row * 64 + (c16 & 3) * 16) = rv[i]; } } while (0)
; __device__ __forceinline__ void attn_unit(const Frame& F, const bf16* __restrict__ proj, bf16* mix, const float* relb, const float* subg, int h, int qb, float lam, float one_m_li) {
;     ...
;     if (tid < 256) { const int rel = tid - 192; lut[tid] = (relb[t5_bucket(rel) * 4 + h] - relb[15 * 4 + h]) * LOG2E; }
;     bf16x8 qr[4];
; #pragma unroll
;     for (int d0 = 0; d0 < 4; ++d0) qr[d0] = *(const bf16x8*)(proj + (size_t)qrow * PW + C_Q + h * 128 + m * 64 + 16 * d0 + 8 * hi);
;     u32x4 rk[2], rv[2];
;     const bf16* kbase = proj + C_K + h * 128; const bf16* vbase = proj + C_V + h * 128;
;     ...
;     AT_LOAD(0);
;     __syncthreads();
;     AT_STORE(0);
;     AT_LOAD(1);
;     __syncthreads();
;     float mrun = 0.f, lsum = 0.f;
;     f32x16 negm = (f32x16){};
;     f32x16 o[4];
; #pragma unroll
;     for (int eb = 0; eb < 4; ++eb) o[eb] = (f32x16){};
;     for (int j = 0; j < NT; ++j) {
;         const int cur = j & 1;
;         bf16x8 kf[2][2];
;         const LAS unsigned char* Kb = lds + cur * STAGE + m * 8192;
;         if (j <= cw) {
; #pragma unroll
;             for (int d0 = 0; d0 < 2; ++d0) { const int c = 2 * d0 + hi; kf[d0][0] = *(const LAS bf16x8*)(Kb + c * 1024 + ((r32 ^ c) * 16)); kf[d0][1] = *(const LAS bf16x8*)(Kb + c * 1024 + ((r32 ^ c) * 16) + 512); } }
.LBB0_573:
	s_or_b64 exec, exec, s[12:13]
	s_movk_i32 s12, 0xc0
	v_cmp_lt_i32_e32 vcc, s12, v32
	s_nop 1
	v_cndmask_b32_e64 v1, 0, 16, vcc
	v_add_lshl_u32 v192, v0, v1, 2
	v_lshl_add_u64 v[0:1], v[192:193], 2, s[46:47]
	global_load_dword v0, v[0:1], off
	s_nop 0
	global_load_dword v1, v193, s[46:47] offset:240
	s_waitcnt vmcnt(0)
	v_sub_f32_e32 v0, v0, v1
	v_lshl_add_u32 v1, v32, 2, 0
	v_mul_f32_e32 v0, 0x3fb8aa3b, v0
	v_add_u32_e32 v1, 0x18000, v1
	ds_write_b32 v1, v0
.LBB0_574:
	s_or_b64 exec, exec, s[10:11]
	s_lshr_b32 s101, s40, 10
	s_xor_b64 s[84:85], s[8:9], -1
	s_and_b64 s[8:9], s[8:9], exec
	s_cselect_b32 s8, s59, s58
	s_lshl_b32 s9, s8, 7
	v_and_b32_e32 v102, 31, v32
	s_or_b32 s9, s9, s29
	v_or_b32_e32 v188, s9, v102
	v_mul_u32_u24_e32 v0, 0x1200, v188
	v_lshlrev_b32_e32 v192, 1, v0
	v_lshl_add_u64 v[0:1], s[42:43], 0, v[192:193]
	v_bfe_u32 v187, v32, 5, 1
	v_lshl_add_u64 v[0:1], s[48:49], 1, v[0:1]
	v_lshl_add_u64 v[0:1], s[4:5], 1, v[0:1]
	v_lshlrev_b32_e32 v192, 4, v187
	v_lshl_add_u64 v[0:1], v[0:1], 0, v[192:193]
	s_mov_b64 s[10:11], 0x39101800
	v_lshl_add_u64 v[2:3], v[0:1], 0, s[10:11]
	s_mov_b32 s10, 0x39101000
	v_add_co_u32_e32 v0, vcc, s10, v0
	v_lshlrev_b32_e32 v33, 4, v32
	s_nop 0
	v_addc_co_u32_e32 v1, vcc, 0, v1, vcc
	v_and_b32_e32 v80, 0xf0, v33
	v_mov_b32_e32 v81, v193
	global_load_dwordx4 v[112:115], v[0:1], off offset:2048
	global_load_dwordx4 v[116:119], v[2:3], off offset:32
	global_load_dwordx4 v[120:123], v[2:3], off offset:64
	global_load_dwordx4 v[124:127], v[2:3], off offset:96
	v_lshl_add_u64 v[2:3], s[80:81], 0, v[80:81]
	v_lshl_add_u64 v[0:1], s[82:83], 0, v[80:81]
	v_ashrrev_i32_e32 v81, 4, v32
	v_mad_i64_i32 v[4:5], s[10:11], v81, s21, v[2:3]
	v_mad_i64_i32 v[8:9], s[10:11], v81, s21, v[0:1]
	v_add_u32_e32 v12, 0x200, v32
	v_ashrrev_i32_e32 v103, 4, v12
	v_mad_i64_i32 v[12:13], s[10:11], v103, s21, v[2:3]
	v_mad_i64_i32 v[16:17], s[10:11], v103, s21, v[0:1]
	v_and_b32_e32 v20, 7, v32
	v_lshlrev_b32_e32 v21, 10, v32
	v_mov_b32_e32 v189, 0
	v_lshlrev_b32_e32 v190, 8, v81
	v_bitop3_b32 v22, v81, v32, 15 bitop3:0x28
	v_add3_u32 v20, 0, v189, v190
	v_and_b32_e32 v191, 0x3000, v21
	v_and_b32_e32 v204, 48, v33
	v_lshlrev_b32_e32 v205, 4, v22
	v_add3_u32 v21, 0, v191, v204
	v_add_u32_e32 v22, v20, v205
	v_lshlrev_b32_e32 v206, 6, v81
	s_waitcnt lgkmcnt(0)
	s_barrier
	v_lshrrev_b32_e32 v4, 6, v32
	v_bfe_u32 v5, v32, 4, 2
	v_lshl_add_u32 v6, v4, 3, v5
	v_and_b32_e32 v7, 15, v32
	v_and_b32_e32 v8, 15, v6
	v_xor_b32_e32 v8, v7, v8
	v_mul_u32_u24_e32 v9, 0x2400, v6
	v_lshl_add_u32 v128, v8, 4, v9
	v_add_u32_e32 v6, 4, v6
	v_and_b32_e32 v8, 15, v6
	v_xor_b32_e32 v8, v7, v8
	v_mul_u32_u24_e32 v9, 0x2400, v6
	v_lshl_add_u32 v129, v8, 4, v9
	v_and_b32_e32 v5, 1, v4
	v_bfe_u32 v6, v32, 2, 4
	v_lshl_add_u32 v6, v5, 5, v6
	v_mul_u32_u24_e32 v9, 0x2400, v6
	v_lshrrev_b32_e32 v5, 1, v4
	v_lshl_add_u32 v9, v5, 6, v9
	v_and_b32_e32 v5, 3, v32
	v_lshl_add_u32 v9, v5, 4, v9
	v_add_u32_e32 v130, 0x400, v9
	v_add_u32_e32 v131, 0x24400, v9
	s_mov_b64 s[50:51], s[80:81]
	s_mov_b32 m0, s100
	s_nop 0
	global_load_lds_dwordx4 v128, s[50:51]
	s_add_i32 m0, s100, 0x400
	s_nop 0
	global_load_lds_dwordx4 v129, s[50:51]
	s_add_i32 m0, s100, 0x4000
	s_nop 0
	global_load_lds_dwordx4 v130, s[50:51]
	s_add_i32 m0, s100, 0x4400
	s_nop 0
	global_load_lds_dwordx4 v131, s[50:51]
	s_add_u32 s50, s50, 0x90000
	s_addc_u32 s51, s51, 0
	s_add_i32 m0, s100, 0x8000
	s_nop 0
	global_load_lds_dwordx4 v128, s[50:51]
	s_add_i32 m0, s100, 0x8400
	s_nop 0
	global_load_lds_dwordx4 v129, s[50:51]
	s_add_i32 m0, s100, 0xc000
	s_nop 0
	global_load_lds_dwordx4 v130, s[50:51]
	s_add_i32 m0, s100, 0xc400
	s_nop 0
	global_load_lds_dwordx4 v131, s[50:51]
	s_add_u32 s50, s50, 0x90000
	s_addc_u32 s51, s51, 0
	v_lshlrev_b32_e32 v208, 6, v103
	v_lshlrev_b32_e32 v209, 8, v102
	v_add_u32_e32 v6, v21, v206
	v_bitop3_b32 v4, v103, v32, 15 bitop3:0x28
	v_add_u32_e32 v9, 64, v81
	v_lshlrev_b32_e32 v207, 4, v4
	v_or_b32_e32 v207, 0x2000, v207
	v_mad_i64_i32 v[4:5], s[10:11], v9, s21, v[2:3]
	v_mad_i64_i32 v[4:5], s[10:11], v9, s21, v[0:1]
	v_add_u32_e32 v9, 64, v103
	v_mad_i64_i32 v[4:5], s[10:11], v9, s21, v[2:3]
	v_mad_i64_i32 v[4:5], s[10:11], v9, s21, v[0:1]
	v_bitop3_b32 v4, v187, v32, 15 bitop3:0x78
	v_xor_b32_e32 v4, s101, v4
	v_lshlrev_b32_e32 v210, 4, v4
	v_add_u32_e32 v7, v20, v207
	v_add_u32_e32 v8, v21, v208
	v_add3_u32 v4, 0, v209, v210
	s_waitcnt vmcnt(4)
	s_waitcnt lgkmcnt(0)
	s_barrier
	ds_read_b128 v[144:147], v4
	ds_read_b128 v[148:151], v4 offset:8192
	v_or_b32_e32 v4, 2, v187
	v_mov_b32_e32 v211, v209
	v_bitop3_b32 v4, v187, v32, 15 bitop3:0x78
	v_xor_b32_e32 v4, s101, v4
	v_xor_b32_e32 v4, 2, v4
	v_lshlrev_b32_e32 v212, 4, v4
	v_add3_u32 v4, 0, v211, v212
	ds_read_b128 v[152:155], v4
	ds_read_b128 v[156:159], v4 offset:8192
	s_cmp_eq_u32 s8, 0
	s_cbranch_scc1 .LBB0_576
	s_add_i32 m0, s100, 0x10000
	s_nop 0
	global_load_lds_dwordx4 v128, s[50:51]
	s_add_i32 m0, s100, 0x10400
	s_nop 0
	global_load_lds_dwordx4 v129, s[50:51]
	s_add_i32 m0, s100, 0x14000
	s_nop 0
	global_load_lds_dwordx4 v130, s[50:51]
	s_add_i32 m0, s100, 0x14400
	s_nop 0
	global_load_lds_dwordx4 v131, s[50:51]
	s_add_u32 s50, s50, 0x90000
	s_addc_u32 s51, s51, 0
; __device__ __forceinline__ void attn_unit(const Frame& F, const bf16* __restrict__ proj, bf16* mix, const float* relb, const float* subg, int h, int qb, float lam, float one_m_li) {
;     ...
;         if (j <= cw) {
;             f32x16 p0, p1;
; #pragma unroll
;             for (int d0 = 0; d0 < 4; ++d0) { const int c = 2 * d0 + hi;
;                 const bf16x8 a0 = (d0 < 2) ? kf[d0 & 1][0] : *(const LAS bf16x8*)(Kb + c * 1024 + ((r32 ^ c) * 16));
;                 const bf16x8 a1 = (d0 < 2) ? kf[d0 & 1][1] : *(const LAS bf16x8*)(Kb + c * 1024 + ((r32 ^ c) * 16) + 512);
;                 if (d0 == 0) { p0 = __builtin_amdgcn_mfma_f32_32x32x16_bf16(a0, qr[0], negm, 0, 0, 0); p1 = __builtin_amdgcn_mfma_f32_32x32x16_bf16(a1, qr[0], negm, 0, 0, 0); }
;                 else { p0 = __builtin_amdgcn_mfma_f32_32x32x16_bf16(a0, qr[d0], p0, 0, 0, 0); p1 = __builtin_amdgcn_mfma_f32_32x32x16_bf16(a1, qr[d0], p1, 0, 0, 0); } }
;             if (j >= cw - 2) {
;                 const int base = 64 * j - qrow + 192;
; #pragma unroll
;                 for (int r = 0; r < 16; ++r) { const int kv = crow(r, hi); p0[r] += lut[base + kv]; p1[r] += lut[base + kv + 32]; }
;             }
;             float mx = fmaxf(fmaxf(p0[0], p0[1]), p1[0]), mb = fmaxf(fmaxf(p0[2], p0[3]), p1[1]); mx = fmaxf(fmaxf(mx, p1[2]), p1[3]);
; #pragma unroll
;             for (int r = 4; r < 16; r += 4) { mx = fmaxf(fmaxf(mx, p0[r]), p0[r + 1]); mb = fmaxf(fmaxf(mb, p0[r + 2]), p0[r + 3]); mx = fmaxf(fmaxf(mx, p1[r]), p1[r + 1]); mb = fmaxf(fmaxf(mb, p1[r + 2]), p1[r + 3]); }
;             mx = swap_max(fmaxf(mx, mb));
;             if (j == 0 || __any(mx > 8.0f)) {
;                 const float dl = (j == 0) ? mx : fmaxf(mx, 0.f); mrun += dl;
;                 const float alpha = __builtin_amdgcn_exp2f(-dl); lsum *= alpha;
; #pragma unroll
;                 for (int r = 0; r < 16; ++r) { p0[r] -= dl; p1[r] -= dl; negm[r] = -mrun; }
; #pragma unroll
;                 for (int eb = 0; eb < 4; ++eb)
; #pragma unroll
;                     for (int r = 0; r < 16; ++r) o[eb][r] *= alpha;
;             }
;             bf16x8 pb[4]; float lpart[4];
;     ...
;             AT_EXPBLK(0);
;             const unsigned vaddr = (unsigned)(uintptr_t)(lds + cur * STAGE + 16384 + (4 * hi + ((lane & 15) >> 2)) * 64 + ((lane >> 4) & 1) * 32 + (lane & 3) * 8);
;             s16x4 fl[2][4], fh[2][4];
;     ...
; #pragma unroll
.LBB0_576:
	s_waitcnt lgkmcnt(3)
	v_mfma_f32_32x32x16_bf16 v[0:15], v[144:147], v[112:115], 0
	v_or_b32_e32 v34, 4, v187
	v_mov_b32_e32 v214, v209
	v_bitop3_b32 v34, v187, v32, 15 bitop3:0x78
	v_xor_b32_e32 v34, s101, v34
	v_xor_b32_e32 v34, 4, v34
	v_lshlrev_b32_e32 v215, 4, v34
	v_add3_u32 v38, 0, v214, v215
	ds_read_b128 v[34:37], v38
	s_cmpk_gt_u32 s9, 0xbf
	s_waitcnt lgkmcnt(2)
	v_mfma_f32_32x32x16_bf16 v[0:15], v[152:155], v[116:119], v[0:15]
	v_mfma_f32_32x32x16_bf16 v[16:31], v[148:151], v[112:115], 0
	s_waitcnt lgkmcnt(0)
	v_mfma_f32_32x32x16_bf16 v[0:15], v[34:37], v[120:123], v[0:15]
	ds_read_b128 v[34:37], v38 offset:8192
	v_mfma_f32_32x32x16_bf16 v[16:31], v[156:159], v[116:119], v[16:31]
	s_waitcnt lgkmcnt(0)
	v_mfma_f32_32x32x16_bf16 v[16:31], v[34:37], v[120:123], v[16:31]
	v_or_b32_e32 v34, 6, v187
	v_mov_b32_e32 v216, v209
	v_bitop3_b32 v34, v187, v32, 15 bitop3:0x78
	v_xor_b32_e32 v34, s101, v34
	v_xor_b32_e32 v34, 6, v34
	v_lshlrev_b32_e32 v217, 4, v34
	v_add3_u32 v38, 0, v216, v217
	ds_read_b128 v[34:37], v38
	s_waitcnt lgkmcnt(0)
	v_mfma_f32_32x32x16_bf16 v[0:15], v[34:37], v[124:127], v[0:15]
	ds_read_b128 v[34:37], v38 offset:8192
	s_waitcnt lgkmcnt(0)
	v_mfma_f32_32x32x16_bf16 v[16:31], v[34:37], v[124:127], v[16:31]
	s_cbranch_scc1 .LBB0_578
	v_lshlrev_b32_e32 v34, 2, v188
	v_sub_u32_e32 v34, 0, v34
	v_add3_u32 v58, v34, v192, s75
	v_add_u32_e32 v58, 0x8000, v58
	ds_read2_b32 v[34:35], v58 offset0:192 offset1:193
	ds_read2_b32 v[36:37], v58 offset0:194 offset1:195
	ds_read2_b32 v[38:39], v58 offset0:200 offset1:201
	ds_read2_b32 v[40:41], v58 offset0:202 offset1:203
	ds_read2_b32 v[42:43], v58 offset0:208 offset1:209
	ds_read2_b32 v[44:45], v58 offset0:210 offset1:211
	ds_read2_b32 v[46:47], v58 offset0:216 offset1:217
	ds_read2_b32 v[48:49], v58 offset0:218 offset1:219
	ds_read2_b32 v[50:51], v58 offset0:224 offset1:225
	ds_read2_b32 v[52:53], v58 offset0:226 offset1:227
	ds_read2_b32 v[54:55], v58 offset0:232 offset1:233
	ds_read2_b32 v[56:57], v58 offset0:234 offset1:235
	s_waitcnt lgkmcnt(4)
	v_pk_add_f32 v[14:15], v[14:15], v[48:49]
	v_pk_add_f32 v[12:13], v[12:13], v[46:47]
	v_pk_add_f32 v[10:11], v[10:11], v[44:45]
	v_pk_add_f32 v[8:9], v[8:9], v[42:43]
	ds_read2_b32 v[42:43], v58 offset0:240 offset1:241
	ds_read2_b32 v[44:45], v58 offset0:242 offset1:243
	ds_read2_b32 v[46:47], v58 offset0:248 offset1:249
	ds_read2_b32 v[48:49], v58 offset0:250 offset1:251
	v_pk_add_f32 v[6:7], v[6:7], v[40:41]
	v_pk_add_f32 v[4:5], v[4:5], v[38:39]
	v_pk_add_f32 v[2:3], v[2:3], v[36:37]
	v_pk_add_f32 v[0:1], v[0:1], v[34:35]
	s_waitcnt lgkmcnt(0)
	v_pk_add_f32 v[30:31], v[30:31], v[48:49]
	v_pk_add_f32 v[28:29], v[28:29], v[46:47]
	v_pk_add_f32 v[26:27], v[26:27], v[44:45]
	v_pk_add_f32 v[24:25], v[24:25], v[42:43]
	v_pk_add_f32 v[22:23], v[22:23], v[56:57]
	v_pk_add_f32 v[20:21], v[20:21], v[54:55]
	v_pk_add_f32 v[18:19], v[18:19], v[52:53]
	v_pk_add_f32 v[16:17], v[16:17], v[50:51]
.LBB0_578:
	v_and_b32_e32 v213, 63, v32
	v_lshlrev_b32_e32 v34, 3, v32
	v_lshlrev_b32_e32 v32, 1, v32
	v_and_b32_e32 v219, 0xc0, v33
	v_and_b32_e32 v220, 32, v32
	s_nop 2
	v_max_f32_e32 v32, v1, v1
	v_max_f32_e32 v33, v0, v0
	v_max_f32_e32 v32, v33, v32
	v_max3_f32 v33, v2, v3, v17
	v_max3_f32 v32, v32, v16, v18
	v_max3_f32 v32, v32, v19, v4
	v_max3_f32 v33, v33, v6, v7
	v_max3_f32 v32, v32, v5, v20
	v_max3_f32 v33, v33, v22, v23
	v_max3_f32 v32, v32, v21, v8
	v_max3_f32 v33, v33, v10, v11
	v_max3_f32 v32, v32, v9, v24
	v_max3_f32 v33, v33, v26, v27
	v_max3_f32 v32, v32, v25, v12
	v_max3_f32 v33, v33, v14, v15
	v_max3_f32 v32, v32, v13, v28
	v_max3_f32 v33, v33, v30, v31
	v_max3_f32 v32, v32, v29, v33
	v_mov_b32_e32 v33, v32
	s_nop 1
	v_permlane32_swap_b32 v32, v33
	v_lshlrev_b32_e32 v218, 8, v187
	v_max_f32_e32 v33, v33, v33
	v_max_f32_e32 v32, v32, v32
	v_max_f32_e32 v82, v32, v33
	v_sub_f32_e32 v0, v0, v82
	v_exp_f32_e32 v84, v0
	v_add_u32_e32 v0, 0, v218
	v_and_b32_e32 v221, 24, v34
	v_sub_f32_e32 v1, v1, v82
	v_add3_u32 v0, v0, v219, v220
	v_sub_f32_e32 v2, v2, v82
	v_sub_f32_e32 v3, v3, v82
	v_sub_f32_e32 v85, v8, v82
	v_exp_f32_e64 v8, -v82
	v_exp_f32_e32 v86, v1
	v_add3_u32 v227, v0, v221, s17
	ds_read_b64_tr_b16 v[0:1], v227 offset:0
	v_sub_f32_e32 v4, v4, v82
	v_sub_f32_e32 v5, v5, v82
	v_exp_f32_e32 v96, v2
	v_exp_f32_e32 v98, v3
	ds_read_b64_tr_b16 v[2:3], v227 offset:512
	v_sub_f32_e32 v6, v6, v82
	v_sub_f32_e32 v7, v7, v82
	v_exp_f32_e32 v92, v4
	v_exp_f32_e32 v94, v5
	ds_read_b64_tr_b16 v[4:5], v227 offset:4096
	v_exp_f32_e32 v88, v6
	v_exp_f32_e32 v90, v7
	ds_read_b64_tr_b16 v[6:7], v227 offset:4608
	v_sub_f32_e32 v97, v9, v82
	v_mul_f32_e32 v64, 0, v8
	ds_read_b64_tr_b16 v[8:9], v227 offset:8192
	v_sub_f32_e32 v99, v10, v82
	v_sub_f32_e32 v100, v11, v82
	ds_read_b64_tr_b16 v[10:11], v227 offset:8704
	ds_read_b64_tr_b16 v[108:109], v227 offset:12288
	ds_read_b64_tr_b16 v[110:111], v227 offset:12800
	ds_read_b64_tr_b16 v[162:163], v227 offset:1024
	ds_read_b64_tr_b16 v[164:165], v227 offset:1536
	ds_read_b64_tr_b16 v[166:167], v227 offset:5120
	ds_read_b64_tr_b16 v[168:169], v227 offset:5632
	ds_read_b64_tr_b16 v[170:171], v227 offset:9216
	ds_read_b64_tr_b16 v[172:173], v227 offset:9728
	ds_read_b64_tr_b16 v[174:175], v227 offset:13312
	ds_read_b64_tr_b16 v[176:177], v227 offset:13824
	s_waitcnt lgkmcnt(8)
; #define AT_TRR(dst, off) asm volatile("ds_read_b64_tr_b16 %0, %1 offset:%c2" : "=&v"(dst) : "v"(vaddr), "i"(off) : "memory")
; #define AT_PIN() do { _Pragma("unroll") for (int g_ = 0; g_ < 4; ++g_) { __builtin_amdgcn_sched_group_barrier(0x008, 1, 0); __builtin_amdgcn_sched_group_barrier(0x400, 2, 0); __builtin_amdgcn_sched_group_barrier(0x002, 2, 0); } \
;                 __builtin_amdgcn_sched_barrier(0); } while (0)
; __device__ __forceinline__ void attn_unit(const Frame& F, const bf16* __restrict__ proj, bf16* mix, const float* relb, const float* subg, int h, int qb, float lam, float one_m_li) {
;     ...
;                 const float dl = (j == 0) ? mx : fmaxf(mx, 0.f); mrun += dl;
;                 const float alpha = __builtin_amdgcn_exp2f(-dl); lsum *= alpha;
; #pragma unroll
;                 for (int r = 0; r < 16; ++r) { p0[r] -= dl; p1[r] -= dl; negm[r] = -mrun; }
; #pragma unroll
;                 for (int eb = 0; eb < 4; ++eb)
; #pragma unroll
;                     for (int r = 0; r < 16; ++r) o[eb][r] *= alpha;
;             }
;             bf16x8 pb[4]; float lpart[4];
;     ...
;             AT_EXPBLK(0);
;             const unsigned vaddr = (unsigned)(uintptr_t)(lds + cur * STAGE + 16384 + (4 * hi + ((lane & 15) >> 2)) * 64 + ((lane >> 4) & 1) * 32 + (lane & 3) * 8);
;             s16x4 fl[2][4], fh[2][4];
;     ...
; #pragma unroll
;             for (int eb = 0; eb < 4; ++eb) { AT_TRR(fl[0][eb], eb * 4096); AT_TRR(fh[0][eb], eb * 4096 + 512); }
;     ...
;             AT_PVSTEP(0); AT_EXPBLK(1); AT_PIN();
;             AT_PVSTEP(1); AT_EXPBLK(2); AT_PIN();
;             AT_PVSTEP(2); AT_EXPBLK(3); AT_PIN();
;             AT_PVSTEP(3); __builtin_amdgcn_sched_barrier(0);
;             lsum += (lpart[0] + lpart[1]) + (lpart[2] + lpart[3]);
	s_lshr_b32 s10, s9, 6
	s_lshl_b32 s12, s8, 1
	s_add_i32 s11, s10, -2
	s_mov_b32 s13, 2
	s_add_i32 s14, s12, 2
	v_mov_b32_e32 v65, v64
	v_mov_b32_e32 v66, v64
	v_mov_b32_e32 v67, v64
	v_mov_b32_e32 v68, v64
	v_mov_b32_e32 v69, v64
	v_mov_b32_e32 v70, v64
	v_mov_b32_e32 v71, v64
	v_mov_b32_e32 v72, v64
	v_mov_b32_e32 v73, v64
	v_mov_b32_e32 v74, v64
	v_mov_b32_e32 v75, v64
	v_mov_b32_e32 v76, v64
	v_mov_b32_e32 v77, v64
	v_mov_b32_e32 v78, v64
	v_mov_b32_e32 v79, v64
	v_sub_f32_e32 v83, v16, v82
	v_sub_f32_e32 v87, v17, v82
	v_sub_f32_e32 v89, v18, v82
	v_sub_f32_e32 v91, v19, v82
	v_sub_f32_e32 v93, v20, v82
	v_sub_f32_e32 v95, v21, v82
	v_sub_f32_e32 v101, v22, v82
	v_sub_f32_e32 v196, v23, v82
	v_sub_f32_e32 v197, v24, v82
	v_sub_f32_e32 v198, v25, v82
	v_sub_f32_e32 v199, v26, v82
	v_sub_f32_e32 v200, v27, v82
	v_sub_f32_e32 v201, v28, v82
	v_sub_f32_e32 v202, v29, v82
	v_sub_f32_e32 v203, v30, v82
	v_sub_f32_e32 v226, v31, v82
	v_sub_f32_e32 v178, v12, v82
	v_sub_f32_e32 v179, v13, v82
	v_sub_f32_e32 v180, v14, v82
	v_sub_f32_e32 v181, v15, v82
	v_cvt_pk_bf16_f32 v104, v84, v86
	v_cvt_pk_bf16_f32 v105, v96, v98
	v_cvt_pk_bf16_f32 v106, v92, v94
	v_cvt_pk_bf16_f32 v107, v88, v90
	s_nop 1
	v_mfma_f32_32x32x16_bf16 v[48:63], v[0:3], v[104:107], v[64:79]
	v_exp_f32_e32 v100, v100
	v_mfma_f32_32x32x16_bf16 v[32:47], v[4:7], v[104:107], v[64:79]
	v_mfma_f32_32x32x16_bf16 v[16:31], v[8:11], v[104:107], v[64:79]
	v_mov_b64_e32 v[0:1], v[64:65]
	v_mov_b64_e32 v[12:13], v[76:77]
	v_mov_b64_e32 v[14:15], v[78:79]
	v_mov_b64_e32 v[8:9], v[72:73]
	v_mov_b64_e32 v[10:11], v[74:75]
	v_mov_b64_e32 v[2:3], v[66:67]
	v_mov_b64_e32 v[4:5], v[68:69]
	v_mov_b64_e32 v[6:7], v[70:71]
	v_exp_f32_e32 v72, v181
	v_exp_f32_e32 v76, v179
	v_exp_f32_e32 v70, v180
	v_exp_f32_e32 v78, v99
	v_exp_f32_e32 v74, v178
	v_mfma_f32_32x32x16_bf16 v[0:15], v[108:111], v[104:107], v[0:15]
	v_exp_f32_e32 v66, v85
	v_exp_f32_e32 v68, v97
	v_cvt_pk_bf16_f32 v105, v78, v100
	v_cvt_pk_bf16_f32 v106, v74, v76
	v_cvt_pk_bf16_f32 v107, v70, v72
	v_cvt_pk_bf16_f32 v104, v66, v68
	ds_read_b64_tr_b16 v[108:109], v227 offset:2048
	ds_read_b64_tr_b16 v[110:111], v227 offset:2560
	ds_read_b64_tr_b16 v[178:179], v227 offset:6144
	ds_read_b64_tr_b16 v[180:181], v227 offset:6656
	ds_read_b64_tr_b16 v[182:183], v227 offset:10240
	ds_read_b64_tr_b16 v[184:185], v227 offset:10752
	ds_read_b64_tr_b16 v[222:223], v227 offset:14336
	ds_read_b64_tr_b16 v[224:225], v227 offset:14848
	s_waitcnt lgkmcnt(8)
	s_nop 1
	v_mfma_f32_32x32x16_bf16 v[48:63], v[162:165], v[104:107], v[48:63]
	v_exp_f32_e32 v85, v83
	v_exp_f32_e32 v87, v87
	s_nop 0
	v_cvt_pk_bf16_f32 v162, v85, v87
	v_mfma_f32_32x32x16_bf16 v[32:47], v[166:169], v[104:107], v[32:47]
	v_exp_f32_e32 v97, v89
	v_exp_f32_e32 v99, v91
	s_nop 0
	v_cvt_pk_bf16_f32 v163, v97, v99
	v_mfma_f32_32x32x16_bf16 v[16:31], v[170:173], v[104:107], v[16:31]
	v_exp_f32_e32 v93, v93
	v_exp_f32_e32 v95, v95
	s_nop 0
	v_cvt_pk_bf16_f32 v164, v93, v95
	v_mfma_f32_32x32x16_bf16 v[0:15], v[174:177], v[104:107], v[0:15]
	v_exp_f32_e32 v89, v101
	v_exp_f32_e32 v91, v196
	s_nop 0
	v_cvt_pk_bf16_f32 v165, v89, v91
	ds_read_b64_tr_b16 v[104:105], v227 offset:3072
	ds_read_b64_tr_b16 v[106:107], v227 offset:3584
	ds_read_b64_tr_b16 v[166:167], v227 offset:7168
	ds_read_b64_tr_b16 v[168:169], v227 offset:7680
	ds_read_b64_tr_b16 v[170:171], v227 offset:11264
	ds_read_b64_tr_b16 v[172:173], v227 offset:11776
	ds_read_b64_tr_b16 v[174:175], v227 offset:15360
	ds_read_b64_tr_b16 v[176:177], v227 offset:15872
	s_waitcnt lgkmcnt(8)
	s_nop 1
	v_mfma_f32_32x32x16_bf16 v[48:63], v[108:111], v[162:165], v[48:63]
	v_exp_f32_e32 v67, v197
	v_exp_f32_e32 v69, v198
	s_nop 0
	v_cvt_pk_bf16_f32 v108, v67, v69
	v_mfma_f32_32x32x16_bf16 v[32:47], v[178:181], v[162:165], v[32:47]
	v_exp_f32_e32 v79, v199
	v_exp_f32_e32 v101, v200
	s_nop 0
	v_cvt_pk_bf16_f32 v109, v79, v101
	v_mfma_f32_32x32x16_bf16 v[16:31], v[182:185], v[162:165], v[16:31]
	v_exp_f32_e32 v75, v201
	v_exp_f32_e32 v77, v202
	s_nop 0
	v_cvt_pk_bf16_f32 v110, v75, v77
	v_mfma_f32_32x32x16_bf16 v[0:15], v[222:225], v[162:165], v[0:15]
	v_exp_f32_e32 v71, v203
	v_exp_f32_e32 v73, v226
	s_nop 0
	v_cvt_pk_bf16_f32 v111, v71, v73
	s_waitcnt lgkmcnt(0)
	s_nop 1
	v_mfma_f32_32x32x16_bf16 v[48:63], v[104:107], v[108:111], v[48:63]
	v_mfma_f32_32x32x16_bf16 v[32:47], v[166:169], v[108:111], v[32:47]
	v_mfma_f32_32x32x16_bf16 v[16:31], v[170:173], v[108:111], v[16:31]
	v_mfma_f32_32x32x16_bf16 v[0:15], v[174:177], v[108:111], v[0:15]
	v_add_f32_e64 v96, v96, v98
	v_add_f32_e64 v97, v97, v99
	v_add_f32_e64 v92, v92, v94
	v_add_f32_e64 v93, v93, v95
	v_add_f32_e64 v88, v88, v90
	v_add_f32_e64 v89, v89, v91
	v_pk_add_f32 v[84:85], v[84:85], v[86:87]
	v_pk_add_f32 v[78:79], v[78:79], v[100:101]
	v_pk_add_f32 v[74:75], v[74:75], v[76:77]
	v_pk_add_f32 v[70:71], v[70:71], v[72:73]
	v_pk_add_f32 v[66:67], v[66:67], v[68:69]
	v_pk_add_f32 v[88:89], v[92:93], v[88:89]
	v_pk_add_f32 v[84:85], v[84:85], v[96:97]
	v_pk_add_f32 v[70:71], v[74:75], v[70:71]
	v_pk_add_f32 v[66:67], v[66:67], v[78:79]
	v_pk_add_f32 v[84:85], v[84:85], v[88:89]
	v_pk_add_f32 v[66:67], v[66:67], v[70:71]
	v_mov_b32_e32 v83, v64
	v_pk_add_f32 v[66:67], v[84:85], v[66:67]
	s_lshl_b32 s15, s8, 9
	v_pk_add_f32 v[66:67], v[66:67], v[66:67] op_sel_hi:[0,1]
	v_mov_b32_e32 v66, v193
	v_pk_add_f32 v[162:163], v[82:83], v[66:67]
	v_mad_i64_i32 v[66:67], s[8:9], v81, s21, 0
	v_pk_add_f32 v[64:65], v[162:163], 0 neg_lo:[1,1] neg_hi:[1,1]
	v_or_b32_e32 v66, v66, v80
	v_lshlrev_b32_e32 v65, 2, v102
	v_sub_u32_e32 v65, v192, v65
	v_lshl_add_u64 v[164:165], s[42:43], 0, v[66:67]
	v_mad_i64_i32 v[66:67], s[8:9], v103, s21, 0
	v_subrev_u32_e32 v65, s15, v65
	v_or_b32_e32 v66, v66, v80
	v_add_u32_e32 v222, s57, v65
	v_lshl_add_u64 v[166:167], s[42:43], 0, v[66:67]
	s_movk_i32 s60, 0xff00
	s_mov_b32 s73, 0x8000
	v_mov_b32_e32 v65, v64
	v_mov_b32_e32 v66, v64
	v_mov_b32_e32 v67, v64
	v_mov_b32_e32 v68, v64
	v_mov_b32_e32 v69, v64
	v_mov_b32_e32 v70, v64
	v_mov_b32_e32 v71, v64
	v_mov_b32_e32 v72, v64
	v_mov_b32_e32 v73, v64
	v_mov_b32_e32 v74, v64
	v_mov_b32_e32 v75, v64
	v_mov_b32_e32 v76, v64
	v_mov_b32_e32 v77, v64
	v_mov_b32_e32 v78, v64
	v_mov_b32_e32 v79, v64
	s_cmp_eq_u32 s12, 0
	s_cbranch_scc1 .Ldma_pw0
	s_waitcnt vmcnt(4)
	s_branch .Ldma_pwd

; __device__ __forceinline__ void attn_unit(const Frame& F, const bf16* __restrict__ proj, bf16* mix, const float* relb, const float* subg, int h, int qb, float lam, float one_m_li) {
;     ...
;     __syncthreads();
;     float mrun = 0.f, lsum = 0.f;
;     f32x16 negm = (f32x16){};
;     f32x16 o[4];
; #pragma unroll
;     for (int eb = 0; eb < 4; ++eb) o[eb] = (f32x16){};
;     for (int j = 0; j < NT; ++j) {
.Ldma_pwd:
	s_barrier
	s_branch .LBB0_581

; #define LAS __attribute__((address_space(3)))
; __device__ __forceinline__ int crow(int r, int hi) { return (r & 3) + 8 * (r >> 2) + 4 * hi; }
; #define AT_LOAD(j) do { _Pragma("unroll") for (int i = 0; i < 2; ++i) { const int id = tid + 512 * i, row = id >> 4, c16 = id & 15; \
;         rk[i] = *(const u32x4*)(kbase + (size_t)(64 * (j) + row) * PW + c16 * 8); rv[i] = *(const u32x4*)(vbase + (size_t)(64 * (j) + row) * PW + c16 * 8); } } while (0)
; __device__ __forceinline__ void attn_unit(const Frame& F, const bf16* __restrict__ proj, bf16* mix, const float* relb, const float* subg, int h, int qb, float lam, float one_m_li) {
;     ...
;     for (int j = 0; j < NT; ++j) {
;         const int cur = j & 1;
;         bf16x8 kf[2][2];
;         const LAS unsigned char* Kb = lds + cur * STAGE + m * 8192;
;         if (j <= cw) {
; #pragma unroll
;             for (int d0 = 0; d0 < 2; ++d0) { const int c = 2 * d0 + hi; kf[d0][0] = *(const LAS bf16x8*)(Kb + c * 1024 + ((r32 ^ c) * 16)); kf[d0][1] = *(const LAS bf16x8*)(Kb + c * 1024 + ((r32 ^ c) * 16) + 512); } }
;         __builtin_amdgcn_sched_barrier(0);
;         if (j + 1 < NT) AT_STORE(cur ^ 1);
;         if (j + 2 < NT) AT_LOAD(j + 2);
;         if (j <= cw) {
;             f32x16 p0, p1;
; #pragma unroll
;             for (int d0 = 0; d0 < 4; ++d0) { const int c = 2 * d0 + hi;
;                 const bf16x8 a0 = (d0 < 2) ? kf[d0 & 1][0] : *(const LAS bf16x8*)(Kb + c * 1024 + ((r32 ^ c) * 16));
;                 const bf16x8 a1 = (d0 < 2) ? kf[d0 & 1][1] : *(const LAS bf16x8*)(Kb + c * 1024 + ((r32 ^ c) * 16) + 512);
;                 if (d0 == 0) { p0 = __builtin_amdgcn_mfma_f32_32x32x16_bf16(a0, qr[0], negm, 0, 0, 0); p1 = __builtin_amdgcn_mfma_f32_32x32x16_bf16(a1, qr[0], negm, 0, 0, 0); }
;                 else { p0 = __builtin_amdgcn_mfma_f32_32x32x16_bf16(a0, qr[d0], p0, 0, 0, 0); p1 = __builtin_amdgcn_mfma_f32_32x32x16_bf16(a1, qr[d0], p1, 0, 0, 0); } }
;             if (j >= cw - 2) {
;                 const int base = 64 * j - qrow + 192;
; #pragma unroll
;                 for (int r = 0; r < 16; ++r) { const int kv = crow(r, hi); p0[r] += lut[base + kv]; p1[r] += lut[base + kv + 32]; }
.LBB0_580:
	s_addk_i32 s60, 0x100
	s_add_i32 s73, s73, 0x8000
	s_cmp_eq_u32 s73, 0x18000
	s_cselect_b32 s73, 0, s73
	s_add_i32 s13, s13, 1
	s_cmp_ge_u32 s86, s12
	s_cbranch_scc1 .Ldma_w0
	s_waitcnt vmcnt(4) lgkmcnt(0)
	s_branch .Ldma_wd
.Ldma_w0:
	s_waitcnt vmcnt(0) lgkmcnt(0)
.Ldma_wd:
	s_barrier
	s_cmp_eq_u32 s15, s60
	s_cbranch_scc1 .LBB0_592
.LBB0_581:
	s_mov_b32 s88, s73
	s_add_i32 s79, s88, 0
	s_add_i32 s86, s13, -1
	s_add_i32 s87, s79, s40
	s_cmp_ge_u32 s86, s12
	s_cbranch_scc1 .Ldma_skip
	s_sub_i32 s101, s88, 0x8000
	s_cmp_eq_u32 s88, 0
	s_cselect_b32 s101, 0x10000, s101
	s_add_i32 s101, s101, s100
	s_mov_b32 m0, s101
	s_nop 0
	global_load_lds_dwordx4 v128, s[50:51]
	s_add_i32 m0, s101, 0x400
	s_nop 0
	global_load_lds_dwordx4 v129, s[50:51]
	s_add_i32 m0, s101, 0x4000
	s_nop 0
	global_load_lds_dwordx4 v130, s[50:51]
	s_add_i32 m0, s101, 0x4400
	s_nop 0
	global_load_lds_dwordx4 v131, s[50:51]
	s_add_u32 s50, s50, 0x90000
	s_addc_u32 s51, s51, 0
.Ldma_skip:
	s_cmp_gt_u32 s86, s10
	s_cbranch_scc1 .LBB0_580
	v_add3_u32 v81, s79, v209, v210
	v_add3_u32 v80, s79, v211, v212
	v_add3_u32 v172, s79, v214, v215
	v_add3_u32 v173, s79, v216, v217
	ds_read_b128 v[144:147], v81
	ds_read_b128 v[148:151], v81 offset:8192
	ds_read_b128 v[152:155], v80
	ds_read_b128 v[156:159], v80 offset:8192
	ds_read_b128 v[168:171], v172
	ds_read_b128 v[176:179], v172 offset:8192
	ds_read_b128 v[180:183], v173
	ds_read_b128 v[196:199], v173 offset:8192
	s_waitcnt lgkmcnt(7)
	v_mfma_f32_32x32x16_bf16 v[96:111], v[144:147], v[112:115], v[64:79]
	s_waitcnt lgkmcnt(6)
	v_mfma_f32_32x32x16_bf16 v[80:95], v[148:151], v[112:115], v[64:79]
	s_waitcnt lgkmcnt(5)
	v_mfma_f32_32x32x16_bf16 v[96:111], v[152:155], v[116:119], v[96:111]
	s_waitcnt lgkmcnt(4)
	v_mfma_f32_32x32x16_bf16 v[80:95], v[156:159], v[116:119], v[80:95]
	s_waitcnt lgkmcnt(3)
	v_mfma_f32_32x32x16_bf16 v[96:111], v[168:171], v[120:123], v[96:111]
	s_waitcnt lgkmcnt(2)
	v_mfma_f32_32x32x16_bf16 v[80:95], v[176:179], v[120:123], v[80:95]
	s_waitcnt lgkmcnt(1)
	v_mfma_f32_32x32x16_bf16 v[96:111], v[180:183], v[124:127], v[96:111]
	s_waitcnt lgkmcnt(0)
	v_mfma_f32_32x32x16_bf16 v[80:95], v[196:199], v[124:127], v[80:95]
	s_cmp_lt_i32 s86, s11
	s_cbranch_scc1 .LBB0_590
	v_add_u32_e32 v223, s60, v222
	v_add_u32_e32 v168, 0x18500, v223
	v_add_u32_e32 v170, 0x18580, v223
	ds_read2_b32 v[168:169], v168 offset1:1
	ds_read2_b32 v[170:171], v170 offset1:1
	v_add_u32_e32 v172, 0x18508, v223
	v_add_u32_e32 v174, 0x18588, v223
	v_add_u32_e32 v176, 0x18520, v223
	v_add_u32_e32 v178, 0x185a0, v223
	v_add_u32_e32 v180, 0x18528, v223
	v_add_u32_e32 v182, 0x185a8, v223
	v_add_u32_e32 v184, 0x18540, v223
	v_add_u32_e32 v196, 0x185c0, v223
	v_add_u32_e32 v198, 0x18548, v223
	v_add_u32_e32 v200, 0x185c8, v223
	v_add_u32_e32 v202, 0x18560, v223
	v_add_u32_e32 v224, 0x185e0, v223
	v_add_u32_e32 v226, 0x18568, v223
	v_add_u32_e32 v223, 0x185e8, v223
	ds_read2_b32 v[172:173], v172 offset1:1
	ds_read2_b32 v[174:175], v174 offset1:1
	ds_read2_b32 v[176:177], v176 offset1:1
	ds_read2_b32 v[178:179], v178 offset1:1
	ds_read2_b32 v[180:181], v180 offset1:1
	ds_read2_b32 v[182:183], v182 offset1:1
	ds_read2_b32 v[184:185], v184 offset1:1
	ds_read2_b32 v[196:197], v196 offset1:1
	ds_read2_b32 v[198:199], v198 offset1:1
	ds_read2_b32 v[200:201], v200 offset1:1
	ds_read2_b32 v[202:203], v202 offset1:1
	ds_read2_b32 v[224:225], v224 offset1:1
	ds_read2_b32 v[226:227], v226 offset1:1
	s_waitcnt lgkmcnt(14)
	v_pk_add_f32 v[96:97], v[96:97], v[168:169]
	ds_read2_b32 v[168:169], v223 offset1:1
	s_waitcnt lgkmcnt(3)
	v_pk_add_f32 v[108:109], v[108:109], v[202:203]
	v_pk_add_f32 v[106:107], v[106:107], v[198:199]
	s_waitcnt lgkmcnt(1)
	v_pk_add_f32 v[110:111], v[110:111], v[226:227]
	v_pk_add_f32 v[104:105], v[104:105], v[184:185]
	v_pk_add_f32 v[102:103], v[102:103], v[180:181]
	v_pk_add_f32 v[100:101], v[100:101], v[176:177]
	v_pk_add_f32 v[98:99], v[98:99], v[172:173]
	s_waitcnt lgkmcnt(0)
	v_pk_add_f32 v[94:95], v[94:95], v[168:169]
	v_pk_add_f32 v[92:93], v[92:93], v[224:225]
	v_pk_add_f32 v[90:91], v[90:91], v[200:201]
	v_pk_add_f32 v[88:89], v[88:89], v[196:197]
	v_pk_add_f32 v[86:87], v[86:87], v[182:183]
	v_pk_add_f32 v[84:85], v[84:85], v[178:179]
	v_pk_add_f32 v[82:83], v[82:83], v[174:175]
	v_pk_add_f32 v[80:81], v[80:81], v[170:171]

; __global__ void __launch_bounds__(NTHR, 2) fwd(Args args) {
	.amdhsa_kernel _Z3fwd4Args
		.amdhsa_group_segment_fixed_size 0
		.amdhsa_private_segment_fixed_size 0
		.amdhsa_kernarg_size 552
		.amdhsa_user_sgpr_count 2
		.amdhsa_user_sgpr_dispatch_ptr 0
		.amdhsa_user_sgpr_queue_ptr 0
		.amdhsa_user_sgpr_kernarg_segment_ptr 1
		.amdhsa_user_sgpr_dispatch_id 0
		.amdhsa_user_sgpr_kernarg_preload_length 0
		.amdhsa_user_sgpr_kernarg_preload_offset 0
		.amdhsa_user_sgpr_private_segment_size 0
		.amdhsa_uses_dynamic_stack 0
		.amdhsa_enable_private_segment 0
		.amdhsa_system_sgpr_workgroup_id_x 1
		.amdhsa_system_sgpr_workgroup_id_y 0
		.amdhsa_system_sgpr_workgroup_id_z 0
		.amdhsa_system_sgpr_workgroup_info 0
		.amdhsa_system_vgpr_workitem_id 0
		.amdhsa_next_free_vgpr 256
		.amdhsa_next_free_sgpr 102
		.amdhsa_accum_offset 256
		.amdhsa_reserve_vcc 1
		.amdhsa_float_round_mode_32 0
		.amdhsa_float_round_mode_16_64 0
		.amdhsa_float_denorm_mode_32 3
		.amdhsa_float_denorm_mode_16_64 3
		.amdhsa_dx10_clamp 1
		.amdhsa_ieee_mode 1
		.amdhsa_fp16_overflow 0
		.amdhsa_tg_split 0
		.amdhsa_exception_fp_ieee_invalid_op 0
		.amdhsa_exception_fp_denorm_src 0
		.amdhsa_exception_fp_ieee_div_zero 0
		.amdhsa_exception_fp_ieee_overflow 0
		.amdhsa_exception_fp_ieee_underflow 0
		.amdhsa_exception_fp_ieee_inexact 0
		.amdhsa_exception_int_div_zero 0
	.end_amdhsa_kernel

; __global__ void __launch_bounds__(NTHR, 2) fwd(Args args) {
amdhsa.kernels:
  - .agpr_count:     0
    .args:
      - .offset:         0
        .size:           296
        .value_kind:     by_value
      - .offset:         296
        .size:           4
        .value_kind:     hidden_block_count_x
      - .offset:         300
        .size:           4
        .value_kind:     hidden_block_count_y
      - .offset:         304
        .size:           4
        .value_kind:     hidden_block_count_z
      - .offset:         308
        .size:           2
        .value_kind:     hidden_group_size_x
      - .offset:         310
        .size:           2
        .value_kind:     hidden_group_size_y
      - .offset:         312
        .size:           2
        .value_kind:     hidden_group_size_z
      - .offset:         314
        .size:           2
        .value_kind:     hidden_remainder_x
      - .offset:         316
        .size:           2
        .value_kind:     hidden_remainder_y
      - .offset:         318
        .size:           2
        .value_kind:     hidden_remainder_z
      - .offset:         336
        .size:           8
        .value_kind:     hidden_global_offset_x
      - .offset:         344
        .size:           8
        .value_kind:     hidden_global_offset_y
      - .offset:         352
        .size:           8
        .value_kind:     hidden_global_offset_z
      - .offset:         360
        .size:           2
        .value_kind:     hidden_grid_dims
      - .offset:         416
        .size:           4
        .value_kind:     hidden_dynamic_lds_size
    .group_segment_fixed_size: 0
    .kernarg_segment_align: 8
    .kernarg_segment_size: 552
    .language:       OpenCL C
    .language_version:
      - 2
      - 0
    .max_flat_workgroup_size: 512
    .name:           _Z3fwd4Args
    .private_segment_fixed_size: 0
    .sgpr_count:     108
    .sgpr_spill_count: 55
    .symbol:         _Z3fwd4Args.kd
    .uniform_work_group_size: 1
    .uses_dynamic_stack: false
    .vgpr_count:     256
    .vgpr_spill_count: 0
    .wavefront_size: 64
